# MoE converter loops: the clamped dangling K-tile prefetch of the last iteration (16 nt loads per wave, 6 percent of an item's HBM reads) is skipped, last-iteration wait variants
# speedup vs baseline: 1.0083x; 1.0083x over previous
; #define G_SCHED __builtin_amdgcn_sched_barrier(0)
; #define CI_LOAD(R, kt) do { _Pragma("unroll") for (int _j = 0; _j < 16; ++_j) R[_j] = __builtin_nontemporal_load((const f32x4*)(src + (size_t)((kt) * 128 + _j) * LDB)); } while (0)
; template <int LDB>
; __device__ __forceinline__ void convert_image(const float* __restrict__ W, int col0, int col1, unsigned char* __restrict__ img, LAS3 char* lds, int wid) {
;     ...
;     f32x4 ra[16], rb[16];
;     CI_LOAD(ra, 0);
;     for (int kt = 0; kt < 16; kt += 2) {
;         CI_LOAD(rb, kt + 1); G_SCHED;
;         CI_CONV(ra, kt); G_SCHED;
;         CI_LOAD(ra, (kt + 2 < 16) ? kt + 2 : 15); G_SCHED;
.Lcw_gu:
	s_waitcnt vmcnt(34)
	v_cvt_scalef32_pk_fp8_f32 v152, v0, v4, s22
	s_waitcnt vmcnt(30)
	v_cvt_scalef32_pk_fp8_f32 v153, v16, v20, s22
	s_waitcnt vmcnt(26)
	v_cvt_scalef32_pk_fp8_f32 v154, v32, v36, s22
	s_waitcnt vmcnt(22)
	v_cvt_scalef32_pk_fp8_f32 v155, v48, v52, s22
	v_cvt_scalef32_pk_fp8_f32 v152, v8, v12, s22 op_sel:[0,0,0,1]
	v_cvt_scalef32_pk_fp8_f32 v153, v24, v28, s22 op_sel:[0,0,0,1]
	v_cvt_scalef32_pk_fp8_f32 v154, v40, v44, s22 op_sel:[0,0,0,1]
	s_waitcnt vmcnt(20)
	v_cvt_scalef32_pk_fp8_f32 v155, v56, v60, s22 op_sel:[0,0,0,1]
	ds_write_b128 v141, v[152:155]
	v_mov_b32_e32 v152, v123
	v_mov_b32_e32 v153, v123
	v_mov_b32_e32 v154, v123
	v_mov_b32_e32 v155, v123
	v_cvt_scalef32_pk_fp8_f32 v152, v1, v5, s22
	v_cvt_scalef32_pk_fp8_f32 v153, v17, v21, s22
	v_cvt_scalef32_pk_fp8_f32 v154, v33, v37, s22
	v_cvt_scalef32_pk_fp8_f32 v155, v49, v53, s22
	v_cvt_scalef32_pk_fp8_f32 v152, v9, v13, s22 op_sel:[0,0,0,1]
	v_cvt_scalef32_pk_fp8_f32 v153, v25, v29, s22 op_sel:[0,0,0,1]
	v_cvt_scalef32_pk_fp8_f32 v154, v41, v45, s22 op_sel:[0,0,0,1]
	v_cvt_scalef32_pk_fp8_f32 v155, v57, v61, s22 op_sel:[0,0,0,1]
	ds_write_b128 v141, v[152:155] offset:128
	v_mov_b32_e32 v152, v123
	v_mov_b32_e32 v0, v123
	v_cvt_scalef32_pk_fp8_f32 v152, v2, v6, s22
	v_mov_b32_e32 v153, v123
	v_mov_b32_e32 v154, v123
	v_mov_b32_e32 v155, v123
	v_cvt_scalef32_pk_fp8_f32 v0, v3, v7, s22
	v_mov_b32_e32 v1, v123
	v_mov_b32_e32 v2, v123
	v_mov_b32_e32 v3, v123
	v_cvt_scalef32_pk_fp8_f32 v153, v18, v22, s22
	v_cvt_scalef32_pk_fp8_f32 v154, v34, v38, s22
	v_cvt_scalef32_pk_fp8_f32 v155, v50, v54, s22
	v_cvt_scalef32_pk_fp8_f32 v1, v19, v23, s22
	v_cvt_scalef32_pk_fp8_f32 v2, v35, v39, s22
	v_cvt_scalef32_pk_fp8_f32 v3, v51, v55, s22
	v_cvt_scalef32_pk_fp8_f32 v152, v10, v14, s22 op_sel:[0,0,0,1]
	v_cvt_scalef32_pk_fp8_f32 v153, v26, v30, s22 op_sel:[0,0,0,1]
	v_cvt_scalef32_pk_fp8_f32 v154, v42, v46, s22 op_sel:[0,0,0,1]
	v_cvt_scalef32_pk_fp8_f32 v155, v58, v62, s22 op_sel:[0,0,0,1]
	v_cvt_scalef32_pk_fp8_f32 v0, v11, v15, s22 op_sel:[0,0,0,1]
	v_cvt_scalef32_pk_fp8_f32 v1, v27, v31, s22 op_sel:[0,0,0,1]
	v_cvt_scalef32_pk_fp8_f32 v2, v43, v47, s22 op_sel:[0,0,0,1]
	v_cvt_scalef32_pk_fp8_f32 v3, v59, v63, s22 op_sel:[0,0,0,1]
	ds_write_b128 v142, v[152:155]
	ds_write_b128 v143, v[0:3]
	s_waitcnt lgkmcnt(0)
	s_barrier
	ds_read_b128 v[0:3], v144
	s_waitcnt lgkmcnt(0)
	s_nop 4
	global_store_dwordx4 v137, v[0:3], s[0:1] sc1
	s_nop 1
	ds_read_b128 v[0:3], v144 offset:1024
	s_waitcnt lgkmcnt(0)
	s_nop 4
	global_store_dwordx4 v138, v[0:3], s[0:1] sc1
	s_nop 1
	ds_read_b128 v[0:3], v144 offset:2048
	s_waitcnt lgkmcnt(0)
	s_nop 4
	global_store_dwordx4 v139, v[0:3], s[0:1] sc1
	s_nop 1
	ds_read_b128 v[0:3], v144 offset:3072
	s_waitcnt lgkmcnt(0)
	s_nop 4
	global_store_dwordx4 v140, v[0:3], s[0:1] sc1
	s_nop 1
	s_cmp_eq_u32 s13, 14
	s_cbranch_scc1 .Lnp_gu
	s_min_u32 s4, s13, 13
	s_lshl_b32 s4, s4, 21
	v_lshl_add_u64 v[56:57], v[132:133], 0, s[4:5]
	s_mov_b32 s4, 0x400000
	v_add_co_u32_e32 v0, vcc, s4, v56
	s_mov_b32 s4, 0x404000
	s_nop 0
	v_addc_co_u32_e32 v1, vcc, 0, v57, vcc
	v_add_co_u32_e32 v4, vcc, s4, v56
	s_mov_b32 s4, 0x408000
	s_nop 0
	v_addc_co_u32_e32 v5, vcc, 0, v57, vcc
	v_add_co_u32_e32 v8, vcc, s4, v56
	s_mov_b32 s4, 0x40c000
	s_nop 0
	v_addc_co_u32_e32 v9, vcc, 0, v57, vcc
	v_add_co_u32_e32 v12, vcc, s4, v56
	s_mov_b32 s4, 0x410000
	s_nop 0
	v_addc_co_u32_e32 v13, vcc, 0, v57, vcc
	v_add_co_u32_e32 v16, vcc, s4, v56
	s_mov_b32 s4, 0x414000
	s_nop 0
	v_addc_co_u32_e32 v17, vcc, 0, v57, vcc
	v_add_co_u32_e32 v20, vcc, s4, v56
	s_mov_b32 s4, 0x418000
	s_nop 0
	v_addc_co_u32_e32 v21, vcc, 0, v57, vcc
	v_add_co_u32_e32 v24, vcc, s4, v56
	s_mov_b32 s4, 0x41c000
	s_nop 0
	v_addc_co_u32_e32 v25, vcc, 0, v57, vcc
	v_add_co_u32_e32 v28, vcc, s4, v56
	s_mov_b32 s4, 0x420000
	s_nop 0
	v_addc_co_u32_e32 v29, vcc, 0, v57, vcc
	v_add_co_u32_e32 v32, vcc, s4, v56
	s_mov_b32 s4, 0x424000
	s_nop 0
	v_addc_co_u32_e32 v33, vcc, 0, v57, vcc
	v_add_co_u32_e32 v36, vcc, s4, v56
	s_mov_b32 s4, 0x428000
	s_nop 0
	v_addc_co_u32_e32 v37, vcc, 0, v57, vcc
	v_add_co_u32_e32 v40, vcc, s4, v56
	s_mov_b32 s4, 0x42c000
	s_nop 0
	v_addc_co_u32_e32 v41, vcc, 0, v57, vcc
	v_add_co_u32_e32 v44, vcc, s4, v56
	s_mov_b32 s4, 0x430000
	s_nop 0
	v_addc_co_u32_e32 v45, vcc, 0, v57, vcc
	v_add_co_u32_e32 v48, vcc, s4, v56
	s_mov_b32 s4, 0x434000
	s_nop 0
	v_addc_co_u32_e32 v49, vcc, 0, v57, vcc
	v_add_co_u32_e32 v52, vcc, s4, v56
	s_mov_b32 s4, 0x438000
	s_nop 0
	v_addc_co_u32_e32 v53, vcc, 0, v57, vcc
	v_add_co_u32_e32 v58, vcc, s4, v56
	s_mov_b32 s4, 0x43c000
	s_nop 0
	v_addc_co_u32_e32 v59, vcc, 0, v57, vcc
	v_add_co_u32_e32 v60, vcc, s4, v56
	global_load_dwordx4 v[0:3], v[0:1], off nt
	s_nop 0
	global_load_dwordx4 v[4:7], v[4:5], off nt
	v_addc_co_u32_e32 v61, vcc, 0, v57, vcc
	global_load_dwordx4 v[8:11], v[8:9], off nt
	s_nop 0
	global_load_dwordx4 v[12:15], v[12:13], off nt
	s_nop 0
	global_load_dwordx4 v[16:19], v[16:17], off nt
	s_nop 0
	global_load_dwordx4 v[20:23], v[20:21], off nt
	s_nop 0
	global_load_dwordx4 v[24:27], v[24:25], off nt
	s_nop 0
	global_load_dwordx4 v[28:31], v[28:29], off nt
	s_nop 0
	global_load_dwordx4 v[32:35], v[32:33], off nt
	s_nop 0
	global_load_dwordx4 v[36:39], v[36:37], off nt
	s_nop 0
	global_load_dwordx4 v[40:43], v[40:41], off nt
	s_nop 0
	global_load_dwordx4 v[44:47], v[44:45], off nt
	s_nop 0
	global_load_dwordx4 v[48:51], v[48:49], off nt
	s_nop 0
	global_load_dwordx4 v[52:55], v[52:53], off nt
	s_nop 0
	global_load_dwordx4 v[56:59], v[58:59], off nt
	s_nop 0
	global_load_dwordx4 v[60:63], v[60:61], off nt
; #define G_SCHED __builtin_amdgcn_sched_barrier(0)
; #define CI_LOAD(R, kt) do { _Pragma("unroll") for (int _j = 0; _j < 16; ++_j) R[_j] = __builtin_nontemporal_load((const f32x4*)(src + (size_t)((kt) * 128 + _j) * LDB)); } while (0)
; template <int LDB>
; __device__ __forceinline__ void convert_image(const float* __restrict__ W, int col0, int col1, unsigned char* __restrict__ img, LAS3 char* lds, int wid) {
;     ...
;     f32x4 ra[16], rb[16];
;     CI_LOAD(ra, 0);
;     for (int kt = 0; kt < 16; kt += 2) {
;         CI_LOAD(rb, kt + 1); G_SCHED;
;         CI_CONV(ra, kt); G_SCHED;
;         CI_LOAD(ra, (kt + 2 < 16) ? kt + 2 : 15); G_SCHED;
;         CI_CONV(rb, kt + 1); G_SCHED;
;     }
.Lnp_gu:
	v_mov_b32_e32 v152, v123
	v_mov_b32_e32 v153, v123
	v_mov_b32_e32 v154, v123
	v_mov_b32_e32 v155, v123
	s_cmp_lg_u32 s13, 14
	s_cbranch_scc1 .Lnw1_gu
	s_waitcnt vmcnt(5)
.Lnw1_gu:
	s_waitcnt vmcnt(21)
	v_cvt_scalef32_pk_fp8_f32 v152, v128, v64, s22
	v_cvt_scalef32_pk_fp8_f32 v153, v76, v80, s22
	v_cvt_scalef32_pk_fp8_f32 v154, v92, v96, s22
	v_cvt_scalef32_pk_fp8_f32 v155, v108, v112, s22
	v_cvt_scalef32_pk_fp8_f32 v152, v68, v72, s22 op_sel:[0,0,0,1]
	v_cvt_scalef32_pk_fp8_f32 v153, v84, v88, s22 op_sel:[0,0,0,1]
	v_cvt_scalef32_pk_fp8_f32 v154, v100, v104, s22 op_sel:[0,0,0,1]
	s_cmp_lg_u32 s13, 14
	s_cbranch_scc1 .Lnw2_gu
	s_waitcnt vmcnt(4)
.Lnw2_gu:
	s_waitcnt vmcnt(20)
	v_cvt_scalef32_pk_fp8_f32 v155, v116, v124, s22 op_sel:[0,0,0,1]
	ds_write_b128 v141, v[152:155] offset:32768
	v_mov_b32_e32 v152, v123
	v_mov_b32_e32 v153, v123
	v_mov_b32_e32 v154, v123
	v_mov_b32_e32 v155, v123
	v_cvt_scalef32_pk_fp8_f32 v152, v129, v65, s22
	v_cvt_scalef32_pk_fp8_f32 v153, v77, v81, s22
	v_cvt_scalef32_pk_fp8_f32 v154, v93, v97, s22
	v_cvt_scalef32_pk_fp8_f32 v155, v109, v113, s22
	v_cvt_scalef32_pk_fp8_f32 v152, v69, v73, s22 op_sel:[0,0,0,1]
	v_cvt_scalef32_pk_fp8_f32 v153, v85, v89, s22 op_sel:[0,0,0,1]
	v_cvt_scalef32_pk_fp8_f32 v154, v101, v105, s22 op_sel:[0,0,0,1]
	v_cvt_scalef32_pk_fp8_f32 v155, v117, v125, s22 op_sel:[0,0,0,1]
	ds_write_b128 v141, v[152:155] offset:32896
	v_mov_b32_e32 v152, v123
	v_mov_b32_e32 v153, v123
	v_mov_b32_e32 v154, v123
	v_mov_b32_e32 v155, v123
	v_mov_b32_e32 v120, v123
	v_mov_b32_e32 v121, v123
	v_mov_b32_e32 v122, v123
	v_cvt_scalef32_pk_fp8_f32 v152, v130, v66, s22
	v_cvt_scalef32_pk_fp8_f32 v153, v78, v82, s22
	v_cvt_scalef32_pk_fp8_f32 v154, v94, v98, s22
	v_cvt_scalef32_pk_fp8_f32 v155, v110, v114, s22
	v_cvt_scalef32_pk_fp8_f32 v120, v131, v67, s22
	v_cvt_scalef32_pk_fp8_f32 v121, v79, v83, s22
	v_cvt_scalef32_pk_fp8_f32 v122, v95, v99, s22
	v_cvt_scalef32_pk_fp8_f32 v123, v111, v115, s22
	v_cvt_scalef32_pk_fp8_f32 v152, v70, v74, s22 op_sel:[0,0,0,1]
	v_cvt_scalef32_pk_fp8_f32 v153, v86, v90, s22 op_sel:[0,0,0,1]
	v_cvt_scalef32_pk_fp8_f32 v154, v102, v106, s22 op_sel:[0,0,0,1]
	v_cvt_scalef32_pk_fp8_f32 v155, v118, v126, s22 op_sel:[0,0,0,1]
	v_cvt_scalef32_pk_fp8_f32 v120, v71, v75, s22 op_sel:[0,0,0,1]
	v_cvt_scalef32_pk_fp8_f32 v121, v87, v91, s22 op_sel:[0,0,0,1]
	v_cvt_scalef32_pk_fp8_f32 v122, v103, v107, s22 op_sel:[0,0,0,1]
	v_cvt_scalef32_pk_fp8_f32 v123, v119, v127, s22 op_sel:[0,0,0,1]
	s_add_u32 s24, s0, 0x8000
	ds_write_b128 v142, v[152:155] offset:32768
	ds_write_b128 v143, v[120:123] offset:32768
	s_waitcnt lgkmcnt(0)
	s_barrier
	ds_read_b128 v[64:67], v144 offset:32768
	s_addc_u32 s25, s1, 0
	s_waitcnt lgkmcnt(0)
	s_nop 4
	global_store_dwordx4 v137, v[64:67], s[24:25] sc1
	s_nop 1
	ds_read_b128 v[64:67], v144 offset:33792
	s_waitcnt lgkmcnt(0)
	s_nop 4
	global_store_dwordx4 v138, v[64:67], s[24:25] sc1
	s_nop 1
	ds_read_b128 v[64:67], v144 offset:34816
	s_waitcnt lgkmcnt(0)
	s_nop 4
	global_store_dwordx4 v139, v[64:67], s[24:25] sc1
	s_nop 1
	ds_read_b128 v[64:67], v144 offset:35840
	s_waitcnt lgkmcnt(0)
	s_nop 4
	global_store_dwordx4 v140, v[64:67], s[24:25] sc1
	s_nop 1
	s_add_u32 s0, s0, 0x10000
	s_addc_u32 s1, s1, 0
	s_mov_b64 s[24:25], 0x400000
	s_cmp_lt_u32 s13, 14
	v_lshl_add_u64 v[134:135], v[134:135], 0, s[24:25]
	s_cbranch_scc1 .LBB0_490

; #define G_SCHED __builtin_amdgcn_sched_barrier(0)
; #define CI_LOAD(R, kt) do { _Pragma("unroll") for (int _j = 0; _j < 16; ++_j) R[_j] = __builtin_nontemporal_load((const f32x4*)(src + (size_t)((kt) * 128 + _j) * LDB)); } while (0)
; template <int LDB>
; __device__ __forceinline__ void convert_image(const float* __restrict__ W, int col0, int col1, unsigned char* __restrict__ img, LAS3 char* lds, int wid) {
;     ...
;     f32x4 ra[16], rb[16];
;     CI_LOAD(ra, 0);
;     for (int kt = 0; kt < 16; kt += 2) {
;         CI_LOAD(rb, kt + 1); G_SCHED;
;         CI_CONV(ra, kt); G_SCHED;
;         CI_LOAD(ra, (kt + 2 < 16) ? kt + 2 : 15); G_SCHED;
.Lcw_dn:
	s_waitcnt vmcnt(34)
	v_cvt_scalef32_pk_fp8_f32 v148, v0, v4, s17
	s_waitcnt vmcnt(30)
	v_cvt_scalef32_pk_fp8_f32 v149, v16, v20, s17
	s_waitcnt vmcnt(26)
	v_cvt_scalef32_pk_fp8_f32 v150, v32, v36, s17
	s_waitcnt vmcnt(22)
	v_cvt_scalef32_pk_fp8_f32 v151, v48, v52, s17
	v_cvt_scalef32_pk_fp8_f32 v148, v8, v12, s17 op_sel:[0,0,0,1]
	v_cvt_scalef32_pk_fp8_f32 v149, v24, v28, s17 op_sel:[0,0,0,1]
	v_cvt_scalef32_pk_fp8_f32 v150, v40, v44, s17 op_sel:[0,0,0,1]
	s_waitcnt vmcnt(20)
	v_cvt_scalef32_pk_fp8_f32 v151, v56, v60, s17 op_sel:[0,0,0,1]
	ds_write_b128 v141, v[148:151]
	v_mov_b32_e32 v148, v123
	v_mov_b32_e32 v149, v123
	v_mov_b32_e32 v150, v123
	v_mov_b32_e32 v151, v123
	v_cvt_scalef32_pk_fp8_f32 v148, v1, v5, s17
	v_cvt_scalef32_pk_fp8_f32 v149, v17, v21, s17
	v_cvt_scalef32_pk_fp8_f32 v150, v33, v37, s17
	v_cvt_scalef32_pk_fp8_f32 v151, v49, v53, s17
	v_cvt_scalef32_pk_fp8_f32 v148, v9, v13, s17 op_sel:[0,0,0,1]
	v_cvt_scalef32_pk_fp8_f32 v149, v25, v29, s17 op_sel:[0,0,0,1]
	v_cvt_scalef32_pk_fp8_f32 v150, v41, v45, s17 op_sel:[0,0,0,1]
	v_cvt_scalef32_pk_fp8_f32 v151, v57, v61, s17 op_sel:[0,0,0,1]
	ds_write_b128 v141, v[148:151] offset:128
	v_mov_b32_e32 v148, v123
	v_mov_b32_e32 v0, v123
	v_cvt_scalef32_pk_fp8_f32 v148, v2, v6, s17
	v_mov_b32_e32 v149, v123
	v_mov_b32_e32 v150, v123
	v_mov_b32_e32 v151, v123
	v_cvt_scalef32_pk_fp8_f32 v0, v3, v7, s17
	v_mov_b32_e32 v1, v123
	v_mov_b32_e32 v2, v123
	v_mov_b32_e32 v3, v123
	v_cvt_scalef32_pk_fp8_f32 v149, v18, v22, s17
	v_cvt_scalef32_pk_fp8_f32 v150, v34, v38, s17
	v_cvt_scalef32_pk_fp8_f32 v151, v50, v54, s17
	v_cvt_scalef32_pk_fp8_f32 v1, v19, v23, s17
	v_cvt_scalef32_pk_fp8_f32 v2, v35, v39, s17
	v_cvt_scalef32_pk_fp8_f32 v3, v51, v55, s17
	v_cvt_scalef32_pk_fp8_f32 v148, v10, v14, s17 op_sel:[0,0,0,1]
	v_cvt_scalef32_pk_fp8_f32 v149, v26, v30, s17 op_sel:[0,0,0,1]
	v_cvt_scalef32_pk_fp8_f32 v150, v42, v46, s17 op_sel:[0,0,0,1]
	v_cvt_scalef32_pk_fp8_f32 v151, v58, v62, s17 op_sel:[0,0,0,1]
	v_cvt_scalef32_pk_fp8_f32 v0, v11, v15, s17 op_sel:[0,0,0,1]
	v_cvt_scalef32_pk_fp8_f32 v1, v27, v31, s17 op_sel:[0,0,0,1]
	v_cvt_scalef32_pk_fp8_f32 v2, v43, v47, s17 op_sel:[0,0,0,1]
	v_cvt_scalef32_pk_fp8_f32 v3, v59, v63, s17 op_sel:[0,0,0,1]
	ds_write_b128 v142, v[148:151]
	ds_write_b128 v143, v[0:3]
	s_waitcnt lgkmcnt(0)
	s_barrier
	ds_read_b128 v[0:3], v152
	s_waitcnt lgkmcnt(0)
	s_nop 4
	global_store_dwordx4 v137, v[0:3], s[0:1] sc1
	s_nop 1
	ds_read_b128 v[0:3], v152 offset:1024
	s_waitcnt lgkmcnt(0)
	s_nop 4
	global_store_dwordx4 v138, v[0:3], s[0:1] sc1
	s_nop 1
	ds_read_b128 v[0:3], v152 offset:2048
	s_waitcnt lgkmcnt(0)
	s_nop 4
	global_store_dwordx4 v139, v[0:3], s[0:1] sc1
	s_nop 1
	ds_read_b128 v[0:3], v152 offset:3072
	s_waitcnt lgkmcnt(0)
	s_nop 4
	global_store_dwordx4 v140, v[0:3], s[0:1] sc1
	s_nop 1
	s_cmp_eq_u32 s14, 14
	s_cbranch_scc1 .Lnp_dn
	s_min_u32 s4, s14, 13
	s_lshl_b32 s4, s4, 20
	v_lshl_add_u64 v[56:57], v[132:133], 0, s[4:5]
	s_mov_b32 s4, 0x200000
	v_add_co_u32_e32 v0, vcc, s4, v56
	s_mov_b32 s4, 0x202000
	s_nop 0
	v_addc_co_u32_e32 v1, vcc, 0, v57, vcc
	v_add_co_u32_e32 v4, vcc, s4, v56
	s_mov_b32 s4, 0x204000
	s_nop 0
	v_addc_co_u32_e32 v5, vcc, 0, v57, vcc
	v_add_co_u32_e32 v8, vcc, s4, v56
	s_mov_b32 s4, 0x206000
	s_nop 0
	v_addc_co_u32_e32 v9, vcc, 0, v57, vcc
	v_add_co_u32_e32 v12, vcc, s4, v56
	s_mov_b32 s4, 0x208000
	s_nop 0
	v_addc_co_u32_e32 v13, vcc, 0, v57, vcc
	v_add_co_u32_e32 v16, vcc, s4, v56
	s_mov_b32 s4, 0x20a000
	s_nop 0
	v_addc_co_u32_e32 v17, vcc, 0, v57, vcc
	v_add_co_u32_e32 v20, vcc, s4, v56
	s_mov_b32 s4, 0x20c000
	s_nop 0
	v_addc_co_u32_e32 v21, vcc, 0, v57, vcc
	v_add_co_u32_e32 v24, vcc, s4, v56
	s_mov_b32 s4, 0x20e000
	s_nop 0
	v_addc_co_u32_e32 v25, vcc, 0, v57, vcc
	v_add_co_u32_e32 v28, vcc, s4, v56
	s_mov_b32 s4, 0x210000
	s_nop 0
	v_addc_co_u32_e32 v29, vcc, 0, v57, vcc
	v_add_co_u32_e32 v32, vcc, s4, v56
	s_mov_b32 s4, 0x212000
	s_nop 0
	v_addc_co_u32_e32 v33, vcc, 0, v57, vcc
	v_add_co_u32_e32 v36, vcc, s4, v56
	s_mov_b32 s4, 0x214000
	s_nop 0
	v_addc_co_u32_e32 v37, vcc, 0, v57, vcc
	v_add_co_u32_e32 v40, vcc, s4, v56
	s_mov_b32 s4, 0x216000
	s_nop 0
	v_addc_co_u32_e32 v41, vcc, 0, v57, vcc
	v_add_co_u32_e32 v44, vcc, s4, v56
	s_mov_b32 s4, 0x218000
	s_nop 0
	v_addc_co_u32_e32 v45, vcc, 0, v57, vcc
	v_add_co_u32_e32 v48, vcc, s4, v56
	s_mov_b32 s4, 0x21a000
	s_nop 0
	v_addc_co_u32_e32 v49, vcc, 0, v57, vcc
	v_add_co_u32_e32 v52, vcc, s4, v56
	s_mov_b32 s4, 0x21c000
	s_nop 0
	v_addc_co_u32_e32 v53, vcc, 0, v57, vcc
	v_add_co_u32_e32 v58, vcc, s4, v56
	s_mov_b32 s4, 0x21e000
	s_nop 0
	v_addc_co_u32_e32 v59, vcc, 0, v57, vcc
	v_add_co_u32_e32 v60, vcc, s4, v56
	global_load_dwordx4 v[0:3], v[0:1], off nt
	s_nop 0
	global_load_dwordx4 v[4:7], v[4:5], off nt
	v_addc_co_u32_e32 v61, vcc, 0, v57, vcc
	global_load_dwordx4 v[8:11], v[8:9], off nt
	s_nop 0
	global_load_dwordx4 v[12:15], v[12:13], off nt
	s_nop 0
	global_load_dwordx4 v[16:19], v[16:17], off nt
	s_nop 0
	global_load_dwordx4 v[20:23], v[20:21], off nt
	s_nop 0
	global_load_dwordx4 v[24:27], v[24:25], off nt
	s_nop 0
	global_load_dwordx4 v[28:31], v[28:29], off nt
	s_nop 0
	global_load_dwordx4 v[32:35], v[32:33], off nt
	s_nop 0
	global_load_dwordx4 v[36:39], v[36:37], off nt
	s_nop 0
	global_load_dwordx4 v[40:43], v[40:41], off nt
	s_nop 0
	global_load_dwordx4 v[44:47], v[44:45], off nt
	s_nop 0
	global_load_dwordx4 v[48:51], v[48:49], off nt
	s_nop 0
	global_load_dwordx4 v[52:55], v[52:53], off nt
	s_nop 0
	global_load_dwordx4 v[56:59], v[58:59], off nt
	s_nop 0
	global_load_dwordx4 v[60:63], v[60:61], off nt
; #define G_SCHED __builtin_amdgcn_sched_barrier(0)
; #define CI_LOAD(R, kt) do { _Pragma("unroll") for (int _j = 0; _j < 16; ++_j) R[_j] = __builtin_nontemporal_load((const f32x4*)(src + (size_t)((kt) * 128 + _j) * LDB)); } while (0)
; template <int LDB>
; __device__ __forceinline__ void convert_image(const float* __restrict__ W, int col0, int col1, unsigned char* __restrict__ img, LAS3 char* lds, int wid) {
;     ...
;     f32x4 ra[16], rb[16];
;     CI_LOAD(ra, 0);
;     for (int kt = 0; kt < 16; kt += 2) {
;         CI_LOAD(rb, kt + 1); G_SCHED;
;         CI_CONV(ra, kt); G_SCHED;
;         CI_LOAD(ra, (kt + 2 < 16) ? kt + 2 : 15); G_SCHED;
;         CI_CONV(rb, kt + 1); G_SCHED;
;     }
.Lnp_dn:
	v_mov_b32_e32 v148, v123
	v_mov_b32_e32 v149, v123
	v_mov_b32_e32 v150, v123
	v_mov_b32_e32 v151, v123
	s_cmp_lg_u32 s14, 14
	s_cbranch_scc1 .Lnw1_dn
	s_waitcnt vmcnt(5)
.Lnw1_dn:
	s_waitcnt vmcnt(21)
	v_cvt_scalef32_pk_fp8_f32 v148, v128, v64, s17
	v_cvt_scalef32_pk_fp8_f32 v149, v76, v80, s17
	v_cvt_scalef32_pk_fp8_f32 v150, v92, v96, s17
	v_cvt_scalef32_pk_fp8_f32 v151, v108, v112, s17
	v_cvt_scalef32_pk_fp8_f32 v148, v68, v72, s17 op_sel:[0,0,0,1]
	v_cvt_scalef32_pk_fp8_f32 v149, v84, v88, s17 op_sel:[0,0,0,1]
	v_cvt_scalef32_pk_fp8_f32 v150, v100, v104, s17 op_sel:[0,0,0,1]
	s_cmp_lg_u32 s14, 14
	s_cbranch_scc1 .Lnw2_dn
	s_waitcnt vmcnt(4)
.Lnw2_dn:
	s_waitcnt vmcnt(20)
	v_cvt_scalef32_pk_fp8_f32 v151, v116, v124, s17 op_sel:[0,0,0,1]
	ds_write_b128 v141, v[148:151] offset:32768
	v_mov_b32_e32 v148, v123
	v_mov_b32_e32 v149, v123
	v_mov_b32_e32 v150, v123
	v_mov_b32_e32 v151, v123
	v_cvt_scalef32_pk_fp8_f32 v148, v129, v65, s17
	v_cvt_scalef32_pk_fp8_f32 v149, v77, v81, s17
	v_cvt_scalef32_pk_fp8_f32 v150, v93, v97, s17
	v_cvt_scalef32_pk_fp8_f32 v151, v109, v113, s17
	v_cvt_scalef32_pk_fp8_f32 v148, v69, v73, s17 op_sel:[0,0,0,1]
	v_cvt_scalef32_pk_fp8_f32 v149, v85, v89, s17 op_sel:[0,0,0,1]
	v_cvt_scalef32_pk_fp8_f32 v150, v101, v105, s17 op_sel:[0,0,0,1]
	v_cvt_scalef32_pk_fp8_f32 v151, v117, v125, s17 op_sel:[0,0,0,1]
	ds_write_b128 v141, v[148:151] offset:32896
	v_mov_b32_e32 v148, v123
	v_mov_b32_e32 v149, v123
	v_mov_b32_e32 v150, v123
	v_mov_b32_e32 v151, v123
	v_mov_b32_e32 v120, v123
	v_mov_b32_e32 v121, v123
	v_mov_b32_e32 v122, v123
	v_cvt_scalef32_pk_fp8_f32 v148, v130, v66, s17
	v_cvt_scalef32_pk_fp8_f32 v149, v78, v82, s17
	v_cvt_scalef32_pk_fp8_f32 v150, v94, v98, s17
	v_cvt_scalef32_pk_fp8_f32 v151, v110, v114, s17
	v_cvt_scalef32_pk_fp8_f32 v120, v131, v67, s17
	v_cvt_scalef32_pk_fp8_f32 v121, v79, v83, s17
	v_cvt_scalef32_pk_fp8_f32 v122, v95, v99, s17
	v_cvt_scalef32_pk_fp8_f32 v123, v111, v115, s17
	v_cvt_scalef32_pk_fp8_f32 v148, v70, v74, s17 op_sel:[0,0,0,1]
	v_cvt_scalef32_pk_fp8_f32 v149, v86, v90, s17 op_sel:[0,0,0,1]
	v_cvt_scalef32_pk_fp8_f32 v150, v102, v106, s17 op_sel:[0,0,0,1]
	v_cvt_scalef32_pk_fp8_f32 v151, v118, v126, s17 op_sel:[0,0,0,1]
	v_cvt_scalef32_pk_fp8_f32 v120, v71, v75, s17 op_sel:[0,0,0,1]
	v_cvt_scalef32_pk_fp8_f32 v121, v87, v91, s17 op_sel:[0,0,0,1]
	v_cvt_scalef32_pk_fp8_f32 v122, v103, v107, s17 op_sel:[0,0,0,1]
	v_cvt_scalef32_pk_fp8_f32 v123, v119, v127, s17 op_sel:[0,0,0,1]
	s_add_u32 s30, s0, 0x8000
	ds_write_b128 v142, v[148:151] offset:32768
	ds_write_b128 v143, v[120:123] offset:32768
	s_waitcnt lgkmcnt(0)
	s_barrier
	ds_read_b128 v[64:67], v152 offset:32768
	s_addc_u32 s31, s1, 0
	s_waitcnt lgkmcnt(0)
	s_nop 4
	global_store_dwordx4 v137, v[64:67], s[30:31] sc1
	s_nop 1
	ds_read_b128 v[64:67], v152 offset:33792
	s_waitcnt lgkmcnt(0)
	s_nop 4
	global_store_dwordx4 v138, v[64:67], s[30:31] sc1
	s_nop 1
	ds_read_b128 v[64:67], v152 offset:34816
	s_waitcnt lgkmcnt(0)
	s_nop 4
	global_store_dwordx4 v139, v[64:67], s[30:31] sc1
	s_nop 1
	ds_read_b128 v[64:67], v152 offset:35840
	s_waitcnt lgkmcnt(0)
	s_nop 4
	global_store_dwordx4 v140, v[64:67], s[30:31] sc1
	s_nop 1
	s_add_u32 s0, s0, 0x10000
	s_addc_u32 s1, s1, 0
	s_mov_b64 s[30:31], 0x200000
	s_cmp_lt_u32 s14, 14
	v_lshl_add_u64 v[134:135], v[134:135], 0, s[30:31]
	s_cbranch_scc1 .LBB0_589
